# LRU pass A item loop: the next item's row prefetch is waited at the back-edge copies (vmcnt(1) behind the first stash store) instead of ~70 instructions after issue; prologue drained before the loop
# baseline (speedup 1.0000x reference)
; __device__ __forceinline__ float softplusf_(float x) { return x > 20.f ? x : 0.6931471805599453f * __builtin_amdgcn_logf(1.f + fexp(x)); }
; template <int PASS>
; __device__ void lru_loop(const Params& p, int l, char* smem, int first, int end, int stride, bool skip_ctx, int oz) {
;     ...
;     const int d = 16 * nt + li, ch = n * 64 + d;
;     bf16x8 wf[2][2];
; #pragma unroll
;     for (int m = 0; m < 2; ++m)
; #pragma unroll
;         for (int s = 0; s < 2; ++s) {
;             const float* W = (m ? p.in[I_LWI] : p.in[I_LWR]) + (size_t)((l * 2 + dir) * 4 + n) * 4096 + d;
;             float w[8];
; #pragma unroll
;             for (int jj = 0; jj < 8; ++jj) w[jj] = W[(32 * s + 8 * g + jj) * 64];
;             u32x4 u = {cvt_pk(w[0], w[1]), cvt_pk(w[2], w[3]), cvt_pk(w[4], w[5]), cvt_pk(w[6], w[7])};
;             wf[m][s] = __builtin_bit_cast(bf16x8, u);
;         }
;     const float br = p.in[I_LBR][(l * 2 + dir) * 256 + ch];
;     const float bi = p.in[I_LBI][(l * 2 + dir) * 256 + ch];
;     const float sp8 = -8.f * 1.4426950408889634f * softplusf_(-p.in[I_LLAM][(l * 2 + dir) * 256 + ch]);
;     float cbv[8], cwv[4][8];
; #pragma unroll
;     for (int e = 0; e < 8; ++e) {
;         cbv[e] = p.in[I_LCB][l * 256 + n * 64 + 8 * c8 + e];
; #pragma unroll
;         for (int j = 0; j < 4; ++j) cwv[j][e] = p.in[I_LCW][(l * 4 + j) * 256 + n * 64 + 8 * c8 + e];
;     }
;     u32x4 nrx[4], nzv = {0u, 0u, 0u, 0u};
;     ...
;     LRU_LOAD(first)
.LBB0_724:
	v_mov_b32_e32 v1, v247
	s_add_i32 s0, s2, s21
	v_add_u32_e32 v60, v1, v197
	s_and_b32 s24, s72, 3
	v_readfirstlane_b32 s1, v60
	s_ashr_i32 s3, s1, 8
	s_lshl_b32 s0, s0, 2
	s_lshl_b32 s26, s3, 2
	s_or_b32 s2, s0, s24
	s_lshl_b32 s0, s21, 2
	s_add_i32 s26, s26, s8
	s_or_b32 s20, s0, s24
	s_ashr_i32 s0, s1, 6
	s_or_b32 s26, s26, s24
	v_and_b32_e32 v63, 15, v60
	s_lshl_b32 s25, s0, 4
	s_ashr_i32 s27, s26, 31
	v_readlane_b32 s36, v253, 2
	v_and_or_b32 v61, s25, 48, v63
	s_lshl_b32 s25, s24, 6
	s_lshl_b64 s[26:27], s[26:27], 14
	v_readlane_b32 s44, v253, 10
	v_readlane_b32 s45, v253, 11
	s_add_u32 s28, s44, s26
	v_bfe_u32 v62, v60, 4, 2
	s_addc_u32 s29, s45, s27
	v_lshlrev_b32_e32 v2, 2, v61
	v_lshl_add_u64 v[4:5], s[28:29], 0, v[2:3]
	v_lshlrev_b32_e32 v6, 11, v62
	v_mov_b32_e32 v7, v3
	v_readlane_b32 s48, v253, 14
	v_lshl_add_u64 v[8:9], v[4:5], 0, v[6:7]
	v_readlane_b32 s49, v253, 15
	global_load_dword v48, v[8:9], off
	global_load_dword v49, v[8:9], off offset:256
	global_load_dword v50, v[8:9], off offset:512
	global_load_dword v51, v[8:9], off offset:768
	global_load_dword v52, v[8:9], off offset:1024
	global_load_dword v53, v[8:9], off offset:1280
	global_load_dword v54, v[8:9], off offset:1536
	global_load_dword v55, v[8:9], off offset:1792
	v_or_b32_e32 v8, 0x2000, v6
	v_mov_b32_e32 v9, v3
	v_or_b32_e32 v12, 0x2100, v6
	v_mov_b32_e32 v13, v3
	v_or_b32_e32 v16, 0x2200, v6
	v_mov_b32_e32 v17, v3
	v_or_b32_e32 v20, 0x2300, v6
	v_mov_b32_e32 v21, v3
	v_or_b32_e32 v24, 0x2400, v6
	v_mov_b32_e32 v25, v3
	v_or_b32_e32 v28, 0x2500, v6
	v_mov_b32_e32 v29, v3
	v_or_b32_e32 v32, 0x2600, v6
	v_mov_b32_e32 v33, v3
	v_or_b32_e32 v36, 0x2700, v6
	v_mov_b32_e32 v37, v3
	s_add_u32 s26, s48, s26
	v_lshl_add_u64 v[10:11], v[4:5], 0, v[8:9]
	v_lshl_add_u64 v[14:15], v[4:5], 0, v[12:13]
	v_lshl_add_u64 v[18:19], v[4:5], 0, v[16:17]
	v_lshl_add_u64 v[22:23], v[4:5], 0, v[20:21]
	v_lshl_add_u64 v[26:27], v[4:5], 0, v[24:25]
	v_lshl_add_u64 v[30:31], v[4:5], 0, v[28:29]
	v_lshl_add_u64 v[34:35], v[4:5], 0, v[32:33]
	v_lshl_add_u64 v[4:5], v[4:5], 0, v[36:37]
	s_addc_u32 s27, s49, s27
	global_load_dword v56, v[10:11], off
	global_load_dword v57, v[14:15], off
	global_load_dword v58, v[18:19], off
	global_load_dword v59, v[22:23], off
	global_load_dword v64, v[26:27], off
	global_load_dword v65, v[30:31], off
	global_load_dword v66, v[34:35], off
	global_load_dword v67, v[4:5], off
	v_lshl_add_u64 v[4:5], s[26:27], 0, v[2:3]
	v_lshl_add_u64 v[6:7], v[4:5], 0, v[6:7]
	s_lshl_b32 s26, s77, 9
	s_and_b32 s27, s1, 0xffffff00
	global_load_dword v68, v[6:7], off
	global_load_dword v69, v[6:7], off offset:256
	global_load_dword v70, v[6:7], off offset:512
	global_load_dword v71, v[6:7], off offset:768
	global_load_dword v72, v[6:7], off offset:1024
	global_load_dword v73, v[6:7], off offset:1280
	global_load_dword v74, v[6:7], off offset:1536
	global_load_dword v75, v[6:7], off offset:1792
	v_lshl_add_u64 v[6:7], v[4:5], 0, v[8:9]
	v_lshl_add_u64 v[8:9], v[4:5], 0, v[12:13]
	v_lshl_add_u64 v[10:11], v[4:5], 0, v[16:17]
	v_lshl_add_u64 v[12:13], v[4:5], 0, v[20:21]
	v_lshl_add_u64 v[14:15], v[4:5], 0, v[24:25]
	v_lshl_add_u64 v[16:17], v[4:5], 0, v[28:29]
	v_lshl_add_u64 v[18:19], v[4:5], 0, v[32:33]
	v_lshl_add_u64 v[4:5], v[4:5], 0, v[36:37]
	v_or_b32_e32 v102, s25, v61
	s_add_i32 s27, s27, s26
	global_load_dword v94, v[6:7], off
	global_load_dword v95, v[8:9], off
	global_load_dword v96, v[10:11], off
	global_load_dword v97, v[12:13], off
	global_load_dword v98, v[14:15], off
	global_load_dword v99, v[16:17], off
	global_load_dword v100, v[18:19], off
	global_load_dword v101, v[4:5], off
	v_or_b32_e32 v4, s27, v102
	v_ashrrev_i32_e32 v5, 31, v4
	v_readlane_b32 s46, v253, 12
	v_readlane_b32 s47, v253, 13
	v_lshlrev_b64 v[4:5], 2, v[4:5]
	v_readlane_b32 s4, v253, 18
	v_and_b32_e32 v38, 7, v60
	v_readlane_b32 s50, v253, 16
	v_readlane_b32 s51, v253, 17
	v_lshl_add_u64 v[6:7], s[46:47], 0, v[4:5]
	v_readlane_b32 s5, v253, 19
	s_lshl_b32 s26, s77, 8
	global_load_dword v1, v[6:7], off
	v_lshl_add_u64 v[6:7], s[50:51], 0, v[4:5]
	v_lshl_add_u64 v[4:5], s[4:5], 0, v[4:5]
	s_or_b32 s26, s25, s26
	v_lshlrev_b32_e32 v2, 3, v38
	global_load_dword v103, v[4:5], off
	v_or_b32_e32 v4, s26, v2
	s_lshl_b32 s26, s77, 10
	s_or_b32 s25, s26, s25
	global_load_dword v134, v[6:7], off
	v_or_b32_e32 v6, s25, v2
	s_mul_hi_i32 s25, s20, 0x38e38e39
	s_lshr_b32 s26, s25, 31
	s_ashr_i32 s25, s25, 5
	s_add_i32 s26, s25, s26
	s_mul_hi_i32 s25, s21, 0x38e38e39
	s_lshr_b32 s27, s25, 31
	s_ashr_i32 s25, s25, 3
	s_add_i32 s25, s25, s27
	s_mul_i32 s25, s25, 36
	s_sub_i32 s21, s21, s25
	s_cmp_lt_i32 s21, 4
	s_cselect_b64 s[28:29], -1, 0
	s_lshl_b32 s21, s21, 6
	v_readlane_b32 s37, v253, 3
	s_add_i32 s25, s21, 0xffffff00
	s_and_b64 s[36:37], s[28:29], exec
	s_cselect_b32 s21, s21, s25
	s_ashr_i32 s27, s26, 31
	s_lshl_b64 s[36:37], s[26:27], 8
	s_add_u32 s25, s36, 0x4000
	v_ashrrev_i32_e32 v135, 3, v60
	s_addc_u32 s31, s37, 0
	s_lshl_b64 s[26:27], s[26:27], 11
	s_and_b64 s[28:29], s[28:29], exec
	s_movk_i32 s4, 0x7ff
	v_add_u32_e32 v46, s21, v135
	s_cselect_b32 s28, 0xff, s4
	v_add_u32_e32 v36, 1, v46
	s_cselect_b32 s27, s31, s27
	s_cselect_b32 s26, s25, s26
	s_lshl_b32 s24, s24, 7
	v_min_i32_e32 v36, s28, v36
	v_cmp_lt_i32_e32 vcc, -2, v46
	s_add_u32 s24, s34, s24
	s_addc_u32 s25, s35, 0
	v_cndmask_b32_e32 v36, 0, v36, vcc
	v_lshlrev_b32_e32 v2, 4, v38
	v_ashrrev_i32_e32 v37, 31, v36
	v_lshl_add_u64 v[92:93], s[24:25], 0, v[2:3]
	v_lshl_add_u64 v[36:37], s[26:27], 0, v[36:37]
	s_mov_b32 s4, 0x100008c0
	v_mad_u64_u32 v[38:39], s[24:25], v36, s92, v[92:93]
	v_min_i32_e32 v36, s28, v46
; template <int PASS>
; __device__ void lru_loop(const Params& p, int l, char* smem, int first, int end, int stride, bool skip_ctx, int oz) {
;     ...
;     LRU_LOAD(first)
;   for (int idx = first; idx < end; idx += stride) {
;     const int item = LRU_ITEM_OF(idx);
;     const int b = item / 144, cid = (item >> 2) % 36;
;     const bool isctx = cid < 4;
;     const int t0 = (isctx ? cid : cid - 4) * 64, Tseg = isctx ? LC : T;
;     const size_t rowbase = isctx ? (size_t)LAT + (size_t)b * LC : (size_t)b * T;
;     u32x4 rx[4];
; #pragma unroll
;     for (int j = 0; j < 4; ++j) rx[j] = nrx[j];
;     ...
;         if (g == 0) *(f32x2*)(AGG + ((size_t)((b * 2 + dir) * 36 + cid) * 256 + ch) * 2) = (f32x2){pc, hc};
;         bf16_t* stp = (bf16_t*)(p.ws + OFF_P) + (size_t)item * 16384 + (size_t)(wave * 4) * 512 + lane * 8;
; #pragma unroll
;         for (int mt = 0; mt < 4; ++mt) {
;             *(u32x4*)(stp + mt * 512) = (u32x4){cvt_pk(hv[mt][0], hv[mt][1]), cvt_pk(hv[mt][2], hv[mt][3]), cvt_pk(pv[mt][0], pv[mt][1]), cvt_pk(pv[mt][2], pv[mt][3])};
;         }
	v_cmp_gt_u32_e32 vcc, s4, v46
	v_mad_i32_i24 v39, v37, s92, v39
	v_readlane_b32 s42, v253, 8
	v_cndmask_b32_e32 v36, 0, v36, vcc
	v_ashrrev_i32_e32 v37, 31, v36
	v_lshl_add_u64 v[36:37], s[26:27], 0, v[36:37]
	v_mad_u64_u32 v[42:43], s[24:25], v36, s92, v[92:93]
	v_add_u32_e32 v36, -1, v46
	v_min_i32_e32 v36, s28, v36
	v_cmp_lt_i32_e32 vcc, 0, v46
	v_readlane_b32 s43, v253, 9
	v_ashrrev_i32_e32 v5, 31, v4
	v_cndmask_b32_e32 v36, 0, v36, vcc
	v_mad_i32_i24 v43, v37, s92, v43
	v_ashrrev_i32_e32 v37, 31, v36
	v_readlane_b32 s40, v253, 6
	v_readlane_b32 s41, v253, 7
	v_lshl_add_u64 v[8:9], v[4:5], 2, s[42:43]
	v_ashrrev_i32_e32 v7, 31, v6
	v_lshl_add_u64 v[36:37], s[26:27], 0, v[36:37]
	v_lshl_add_u64 v[40:41], v[6:7], 2, s[40:41]
	global_load_dwordx4 v[4:7], v[8:9], off offset:16
	s_nop 0
	global_load_dwordx4 v[8:11], v[8:9], off
	s_nop 0
	global_load_dwordx4 v[12:15], v[40:41], off offset:16
	global_load_dwordx4 v[16:19], v[40:41], off
	global_load_dwordx4 v[20:23], v[40:41], off offset:1040
	global_load_dwordx4 v[24:27], v[40:41], off offset:1024
	global_load_dwordx4 v[28:31], v[40:41], off offset:2064
	global_load_dwordx4 v[32:35], v[40:41], off offset:2048
	v_mad_u64_u32 v[44:45], s[24:25], v36, s92, v[92:93]
	v_add_u32_e32 v36, -2, v46
	v_min_i32_e32 v36, s28, v36
	v_cmp_lt_i32_e32 vcc, 1, v46
	v_mad_i32_i24 v45, v37, s92, v45
	s_mov_b32 s21, 0xc1a00000
	v_cndmask_b32_e32 v36, 0, v36, vcc
	v_ashrrev_i32_e32 v37, 31, v36
	v_lshl_add_u64 v[36:37], s[26:27], 0, v[36:37]
	v_mad_u64_u32 v[46:47], s[24:25], v36, s92, v[92:93]
	v_mad_i32_i24 v47, v37, s92, v47
	global_load_dwordx4 v[84:87], v[44:45], off
	global_load_dwordx4 v[88:91], v[46:47], off
	global_load_dwordx4 v[76:79], v[38:39], off
	global_load_dwordx4 v[80:83], v[42:43], off
	s_nop 0
	global_load_dwordx4 v[36:39], v[40:41], off offset:3088
	s_nop 0
	global_load_dwordx4 v[40:43], v[40:41], off offset:3072
	s_waitcnt vmcnt(41)
	v_cvt_pk_bf16_f32 v47, v54, v55
	s_waitcnt vmcnt(15)
	v_mul_f32_e32 v54, 0xbfb8aa3b, v103
	v_cvt_pk_bf16_f32 v44, v48, v49
	v_cvt_pk_bf16_f32 v48, v56, v57
	v_exp_f32_e32 v57, v54
	v_cvt_pk_bf16_f32 v45, v50, v51
	v_cvt_pk_bf16_f32 v50, v64, v65
	s_cmpk_gt_u32 s1, 0xff
	v_add_f32_e32 v57, 1.0, v57
	v_log_f32_e32 v64, v57
	v_cmp_gt_f32_e32 vcc, s21, v103
	s_cselect_b64 s[28:29], -1, 0
	s_lshl_b32 s0, s0, 2
	v_mul_f32_e32 v64, 0xbf317218, v64
	v_cndmask_b32_e32 v64, v64, v103, vcc
	s_movk_i32 s4, 0x90
	s_ashr_i32 s1, s0, 31
	s_ashr_i32 s21, s20, 31
	v_and_b32_e32 v104, 63, v60
	v_mul_f32_e32 v136, 0x4138aa3b, v64
	v_mul_lo_u32 v64, v135, s4
	v_and_b32_e32 v60, 48, v60
	v_readlane_b32 s4, v253, 63
	s_lshl_b64 s[0:1], s[0:1], 10
	s_lshl_b64 s[24:25], s[20:21], 15
	v_cvt_pk_bf16_f32 v51, v66, v67
	v_add_u32_e32 v65, 0, v60
	v_lshl_add_u32 v66, v61, 1, 0
	v_lshlrev_b32_e32 v60, 3, v102
	v_mov_b32_e32 v61, v3
	v_readlane_b32 s5, v254, 0
	s_add_u32 s0, s24, s0
	v_cvt_pk_bf16_f32 v56, v94, v95
	v_lshl_add_u64 v[94:95], s[4:5], 0, v[60:61]
	s_addc_u32 s1, s25, s1
	v_readlane_b32 s4, v255, 37
	v_readlane_b32 s38, v253, 4
	v_readlane_b32 s39, v253, 5
	v_and_or_b32 v60, v236, 64, v63
	s_add_u32 s0, s4, s0
	v_readlane_b32 s4, v255, 38
	v_add_u32_e32 v64, 0, v64
	v_cmp_eq_u32_e64 s[36:37], 2, v62
	v_cmp_eq_u32_e64 s[38:39], 1, v62
	v_cmp_eq_u32_e64 s[42:43], 3, v62
	v_mul_u32_u24_e32 v67, 0x90, v63
	v_mul_u32_u24_e32 v62, 0x240, v62
	v_lshlrev_b32_e32 v137, 2, v60
	v_lshlrev_b32_e32 v60, 4, v104
	s_addc_u32 s1, s4, s1
	v_readlane_b32 s18, v253, 32
	v_readlane_b32 s19, v253, 33
	v_cvt_pk_bf16_f32 v46, v52, v53
	v_cvt_pk_bf16_f32 v52, v68, v69
	v_cvt_pk_bf16_f32 v53, v70, v71
	v_cvt_pk_bf16_f32 v54, v72, v73
	v_cvt_pk_bf16_f32 v55, v74, v75
	v_cvt_pk_bf16_f32 v57, v96, v97
	v_lshl_add_u64 v[96:97], s[0:1], 0, v[60:61]
	v_add_u32_e32 v2, v64, v2
	v_add_u32_e32 v141, v65, v67
	v_add_u32_e32 v142, v66, v62
	v_cvt_pk_bf16_f32 v49, v58, v59
	v_cvt_pk_bf16_f32 v58, v98, v99
	v_cvt_pk_bf16_f32 v59, v100, v101
	v_cmp_gt_u32_e64 s[40:41], 16, v104
	v_or_b32_e32 v138, 0xc0, v137
	v_or_b32_e32 v139, 0x80, v137
	v_or_b32_e32 v140, 64, v137
	s_mov_b64 s[18:19], s[88:89]
	v_readlane_b32 s6, v253, 20
	v_readlane_b32 s7, v253, 21
	v_readlane_b32 s8, v253, 22
	v_readlane_b32 s9, v253, 23
	s_waitcnt vmcnt(5)
	v_mov_b64_e32 v[64:65], v[84:85]
	s_waitcnt vmcnt(4)
	v_mov_b64_e32 v[60:61], v[88:89]
	s_waitcnt vmcnt(3)
	v_mov_b64_e32 v[72:73], v[76:77]
	s_waitcnt vmcnt(2)
	v_mov_b64_e32 v[68:69], v[80:81]
	v_mov_b64_e32 v[62:63], v[90:91]
	v_mov_b64_e32 v[66:67], v[86:87]
	v_mov_b64_e32 v[70:71], v[82:83]
	v_mov_b64_e32 v[74:75], v[78:79]
	v_readlane_b32 s10, v253, 24
	v_readlane_b32 s11, v253, 25
	v_readlane_b32 s12, v253, 26
	v_readlane_b32 s13, v253, 27
	v_readlane_b32 s14, v253, 28
	v_readlane_b32 s15, v253, 29
	v_readlane_b32 s16, v253, 30
	v_readlane_b32 s17, v253, 31
	s_waitcnt vmcnt(0)
	s_branch .LBB0_726
.LBB0_725:
	s_or_b64 exec, exec, s[0:1]
	v_cvt_pk_bf16_f32 v76, v112, v156
	v_cvt_pk_bf16_f32 v77, v106, v130
	v_cvt_pk_bf16_f32 v78, v126, v132
	v_cvt_pk_bf16_f32 v79, v116, v122
	global_store_dwordx4 v[96:97], v[76:79], off offset:-2048
	s_mov_b64 s[0:1], 0x20000
	s_waitcnt vmcnt(1)
	v_mov_b64_e32 v[90:91], v[62:63]
	v_cvt_pk_bf16_f32 v76, v131, v133
	v_cvt_pk_bf16_f32 v77, v104, v124
	v_cvt_pk_bf16_f32 v78, v123, v117
	v_cvt_pk_bf16_f32 v79, v108, v118
	global_store_dwordx4 v[96:97], v[76:79], off offset:-1024
	s_and_b64 vcc, exec, s[44:45]
	v_mov_b64_e32 v[88:89], v[60:61]
	v_cvt_pk_bf16_f32 v76, v125, v127
	v_cvt_pk_bf16_f32 v77, v99, v120
	v_cvt_pk_bf16_f32 v78, v119, v109
	v_cvt_pk_bf16_f32 v79, v110, v114
	global_store_dwordx4 v[96:97], v[76:79], off
	s_mov_b32 s20, s21
	s_nop 0
	v_cvt_pk_bf16_f32 v76, v121, v111
	v_cvt_pk_bf16_f32 v77, v87, v81
	v_cvt_pk_bf16_f32 v78, v115, v105
	v_cvt_pk_bf16_f32 v79, v107, v113
	global_store_dwordx4 v[96:97], v[76:79], off offset:1024
	v_mov_b64_e32 v[86:87], v[66:67]
	v_mov_b64_e32 v[82:83], v[70:71]
	v_mov_b64_e32 v[78:79], v[74:75]
	v_lshl_add_u64 v[96:97], v[96:97], 0, s[0:1]
	v_mov_b64_e32 v[84:85], v[64:65]
	v_mov_b64_e32 v[80:81], v[68:69]
	v_mov_b64_e32 v[76:77], v[72:73]
	s_cbranch_vccnz .LBB0_734

; __device__ __forceinline__ float bf2f(bf16_t v) { return __uint_as_float(((unsigned)v) << 16); }
; template <int PASS>
; __device__ void lru_loop(const Params& p, int l, char* smem, int first, int end, int stride, bool skip_ctx, int oz) {
;     ...
;     {
;         float acc[8];
; #pragma unroll
;         for (int e = 0; e < 8; ++e) acc[e] = cbv[e];
; #pragma unroll
;         for (int j = 0; j < 4; ++j) {
;             const int tt = t0 + ft + j - 2;
;             const bool ok = (tt >= 0) && (tt < Tseg);
; #pragma unroll
;             for (int w = 0; w < 4; ++w) {
;                 const unsigned xw = ok ? rx[j][w] : 0u;
;                 acc[2 * w] += cwv[j][2 * w] * lo16(xw);
;                 acc[2 * w + 1] += cwv[j][2 * w + 1] * hi16(xw);
;             }
;         }
;         u32x4 o = {cvt_pk(acc[0], acc[1]), cvt_pk(acc[2], acc[3]), cvt_pk(acc[4], acc[5]), cvt_pk(acc[6], acc[7])};
;         *(u32x4*)(ul + ft * LS + 8 * c8) = o;
;     }
;     if (PASS == 1) {
; #pragma unroll
;         for (int k = 0; k < 5; ++k) {
;             const int pidx = tid + 512 * k;
;             if (pidx < 2 * 35 * 32) *(f32x4*)(pre + pidx * 4) = pr[k];
;         }
;     }
;     __syncthreads();
;     if (PASS == 1 && tid < 128) {
;         const int dd = tid >> 6, cc = tid & 63, np = dd ? posb : posf;
;         float h = 0.f;
;         for (int q = 0; q < np; ++q) {
;             const f32x2 ah = *(const f32x2*)(pre + ((dd * 35 + q) * 64 + cc) * 2);
;             h = ah[0] * h + ah[1];
;         }
;         car[tid] = h;
;     }
;     float av[4][4], bv[4][4], hv[4][4];
; #pragma unroll
;     for (int mt = 0; mt < 4; ++mt) {
;         f32x4 racc = {0.f, 0.f, 0.f, 0.f}, iacc = {0.f, 0.f, 0.f, 0.f};
; #pragma unroll
;         for (int s = 0; s < 2; ++s) {
;             const bf16x8 a = *(const bf16x8*)(ul + (16 * mt + li) * LS + 32 * s + 8 * g);
;             racc = MFMA32(a, wf[0][s], racc);
;             iacc = MFMA32(a, wf[1][s], iacc);
;         }
; #pragma unroll
;         for (int r = 0; r < 4; ++r) {
;             const float uval = bf2f(ul[(16 * mt + 4 * g + r) * LS + d]);
;             const float rg = sigmoidf_(racc[r] + br), ig = sigmoidf_(iacc[r] + bi);
;             const float a = fexp2(sp8 * rg);
;             av[mt][r] = a;
;             bv[mt][r] = __builtin_amdgcn_sqrtf(fmaxf(0.f, 1.f - a * a)) * ig * uval;
;         }
;     }
.LBB0_728:
	s_ashr_i32 s0, s20, 2
	s_mul_hi_i32 s1, s0, 0x38e38e39
	s_lshr_b32 s24, s1, 31
	s_ashr_i32 s1, s1, 3
	s_add_i32 s1, s1, s24
	s_mul_i32 s1, s1, 36
	s_sub_i32 s24, s0, s1
	s_lshl_b32 s0, s24, 6
	s_add_i32 s1, s0, 0xffffff00
	s_cmp_lt_i32 s24, 4
	s_cselect_b32 s0, s0, s1
	v_add_u32_e32 v110, s0, v135
	s_movk_i32 s0, 0x102
	s_cselect_b32 s25, s0, 0x802
	v_cmp_lt_i32_e32 vcc, 1, v110
	v_cmp_gt_i32_e64 s[0:1], s25, v110
	s_and_b64 vcc, vcc, s[0:1]
	v_add_u32_e32 v102, 1, v110
	v_cndmask_b32_e32 v88, 0, v88, vcc
	v_cndmask_b32_e32 v89, 0, v89, vcc
	v_cndmask_b32_e32 v90, 0, v90, vcc
	v_cndmask_b32_e32 v91, 0, v91, vcc
	v_cmp_lt_i32_e32 vcc, 0, v110
	v_cmp_gt_i32_e64 s[0:1], s25, v102
	s_and_b64 vcc, vcc, s[0:1]
	v_add_u32_e32 v106, 2, v110
	v_cndmask_b32_e32 v84, 0, v84, vcc
	v_cndmask_b32_e32 v85, 0, v85, vcc
	v_cndmask_b32_e32 v86, 0, v86, vcc
	v_cndmask_b32_e32 v87, 0, v87, vcc
	v_cmp_lt_i32_e32 vcc, -1, v110
	v_cmp_gt_i32_e64 s[0:1], s25, v106
	s_and_b64 vcc, vcc, s[0:1]
	v_add_u32_e32 v111, 3, v110
	v_lshlrev_b32_e32 v98, 16, v88
	v_and_b32_e32 v99, 0xffff0000, v88
	v_lshlrev_b32_e32 v88, 16, v89
	v_and_b32_e32 v89, 0xffff0000, v89
	v_cndmask_b32_e32 v80, 0, v80, vcc
	v_cndmask_b32_e32 v81, 0, v81, vcc
	v_cndmask_b32_e32 v82, 0, v82, vcc
	v_cndmask_b32_e32 v83, 0, v83, vcc
	v_cmp_lt_i32_e32 vcc, -2, v110
	v_cmp_gt_i32_e64 s[0:1], s25, v111
	v_lshlrev_b32_e32 v102, 16, v84
	v_and_b32_e32 v103, 0xffff0000, v84
	v_lshlrev_b32_e32 v84, 16, v85
	v_and_b32_e32 v85, 0xffff0000, v85
	s_and_b64 vcc, vcc, s[0:1]
	v_pk_fma_f32 v[88:89], v[18:19], v[88:89], v[10:11]
	v_lshlrev_b32_e32 v100, 16, v90
	v_and_b32_e32 v101, 0xffff0000, v90
	v_lshlrev_b32_e32 v106, 16, v80
	v_and_b32_e32 v107, 0xffff0000, v80
	v_lshlrev_b32_e32 v80, 16, v81
	v_and_b32_e32 v81, 0xffff0000, v81
	v_cndmask_b32_e32 v76, 0, v76, vcc
	v_cndmask_b32_e32 v77, 0, v77, vcc
	v_pk_fma_f32 v[84:85], v[26:27], v[84:85], v[88:89]
	v_lshlrev_b32_e32 v104, 16, v86
	v_and_b32_e32 v105, 0xffff0000, v86
	v_lshlrev_b32_e32 v110, 16, v76
	v_and_b32_e32 v111, 0xffff0000, v76
	v_lshlrev_b32_e32 v76, 16, v77
	v_and_b32_e32 v77, 0xffff0000, v77
	v_pk_fma_f32 v[80:81], v[34:35], v[80:81], v[84:85]
	v_pk_fma_f32 v[84:85], v[12:13], v[100:101], v[4:5]
	v_lshlrev_b32_e32 v108, 16, v82
	v_and_b32_e32 v109, 0xffff0000, v82
	v_pk_fma_f32 v[80:81], v[42:43], v[76:77], v[80:81]
	v_cndmask_b32_e32 v77, 0, v78, vcc
	v_pk_fma_f32 v[84:85], v[20:21], v[104:105], v[84:85]
	v_lshlrev_b32_e32 v90, 16, v91
	v_and_b32_e32 v91, 0xffff0000, v91
	v_lshlrev_b32_e32 v76, 16, v77
	v_and_b32_e32 v77, 0xffff0000, v77
	v_pk_fma_f32 v[84:85], v[28:29], v[108:109], v[84:85]
	v_lshlrev_b32_e32 v86, 16, v87
	v_and_b32_e32 v87, 0xffff0000, v87
	v_pk_fma_f32 v[98:99], v[16:17], v[98:99], v[8:9]
	v_pk_fma_f32 v[84:85], v[36:37], v[76:77], v[84:85]
	v_cndmask_b32_e32 v77, 0, v79, vcc
	v_pk_fma_f32 v[78:79], v[14:15], v[90:91], v[6:7]
	v_lshlrev_b32_e32 v82, 16, v83
	v_and_b32_e32 v83, 0xffff0000, v83
	v_pk_fma_f32 v[98:99], v[24:25], v[102:103], v[98:99]
	v_pk_fma_f32 v[78:79], v[22:23], v[86:87], v[78:79]
	v_pk_fma_f32 v[98:99], v[32:33], v[106:107], v[98:99]
	v_lshlrev_b32_e32 v76, 16, v77
	v_and_b32_e32 v77, 0xffff0000, v77
	v_pk_fma_f32 v[78:79], v[30:31], v[82:83], v[78:79]
	v_pk_fma_f32 v[98:99], v[40:41], v[110:111], v[98:99]
	v_pk_fma_f32 v[82:83], v[38:39], v[76:77], v[78:79]
	v_cvt_pk_bf16_f32 v76, v98, v99
	v_cvt_pk_bf16_f32 v77, v80, v81
	v_cvt_pk_bf16_f32 v78, v84, v85
	v_cvt_pk_bf16_f32 v79, v82, v83
	s_barrier
	ds_write_b128 v2, v[76:79]
	s_waitcnt lgkmcnt(0)
	s_barrier
	ds_read_b128 v[76:79], v141
	ds_read_b128 v[80:83], v141 offset:64
	s_waitcnt lgkmcnt(1)
	v_mfma_f32_16x16x32_bf16 v[84:87], v[76:79], v[44:47], 0
	s_mov_b64 s[0:1], -1
	s_and_b64 vcc, exec, s[28:29]
	s_waitcnt lgkmcnt(0)
	v_mfma_f32_16x16x32_bf16 v[84:87], v[80:83], v[48:51], v[84:87]
	v_mfma_f32_16x16x32_bf16 v[76:79], v[76:79], v[52:55], 0
	v_mfma_f32_16x16x32_bf16 v[78:81], v[80:83], v[56:59], v[76:79]
	s_nop 5
	v_add_f32_e32 v84, v1, v84
	v_mul_f32_e32 v84, 0xbfb8aa3b, v84
	v_exp_f32_e32 v84, v84
	s_nop 0
	v_add_f32_e32 v76, 1.0, v84
	v_rcp_f32_e32 v76, v76
	v_add_f32_e32 v77, v134, v78
	v_add_f32_e32 v84, v1, v85
	v_mul_f32_e32 v77, 0xbfb8aa3b, v77
	v_mul_f32_e32 v76, v136, v76
	v_exp_f32_e32 v76, v76
	v_mul_f32_e32 v84, 0xbfb8aa3b, v84
	v_exp_f32_e32 v77, v77
	v_exp_f32_e32 v84, v84
	v_fma_f32 v85, -v76, v76, 1.0
	v_max_f32_e32 v85, 0, v85
	v_add_f32_e32 v77, 1.0, v77
	v_add_f32_e32 v84, 1.0, v84
	v_rcp_f32_e32 v77, v77
	v_sqrt_f32_e32 v85, v85
	v_rcp_f32_e32 v84, v84
	v_add_f32_e32 v79, v134, v79
	v_mul_f32_e32 v79, 0xbfb8aa3b, v79
	v_mul_f32_e32 v77, v77, v85
	v_mul_f32_e32 v84, v136, v84
	v_add_f32_e32 v85, v1, v86
	v_exp_f32_e32 v144, v84
	v_mul_f32_e32 v85, 0xbfb8aa3b, v85
	v_exp_f32_e32 v79, v79
	v_exp_f32_e32 v85, v85
	ds_read_u16 v78, v142
	ds_read_u16 v82, v142 offset:144
	ds_read_u16 v83, v142 offset:288
	ds_read_u16 v104, v142 offset:432
	ds_read_u16 v105, v142 offset:2304
	ds_read_u16 v106, v142 offset:2448
	ds_read_u16 v107, v142 offset:2592
	ds_read_u16 v110, v142 offset:2736
	s_waitcnt lgkmcnt(7)
	v_lshlrev_b32_e32 v78, 16, v78
	v_fma_f32 v84, -v144, v144, 1.0
	v_add_f32_e32 v79, 1.0, v79
	v_max_f32_e32 v84, 0, v84
	v_mul_f32_e32 v78, v77, v78
	s_waitcnt lgkmcnt(6)
	v_lshlrev_b32_e32 v77, 16, v82
	v_add_f32_e32 v82, 1.0, v85
	v_add_f32_e32 v80, v134, v80
	v_rcp_f32_e32 v79, v79
	v_sqrt_f32_e32 v84, v84
	v_rcp_f32_e32 v82, v82
	v_mul_f32_e32 v80, 0xbfb8aa3b, v80
	v_exp_f32_e32 v80, v80
	v_mul_f32_e32 v79, v79, v84
	v_mul_f32_e32 v82, v136, v82
	v_exp_f32_e32 v145, v82
	v_mul_f32_e32 v143, v79, v77
	v_add_f32_e32 v77, 1.0, v80
	v_add_f32_e32 v80, v1, v87
	ds_read_b128 v[84:87], v141 offset:2304
	ds_read_b128 v[88:91], v141 offset:2368
	v_fma_f32 v79, -v145, v145, 1.0
	v_max_f32_e32 v79, 0, v79
	v_rcp_f32_e32 v77, v77
	v_sqrt_f32_e32 v79, v79
	v_mul_f32_e32 v80, 0xbfb8aa3b, v80
	v_exp_f32_e32 v82, v80
	s_waitcnt lgkmcnt(1)
; __device__ __forceinline__ float bf2f(bf16_t v) { return __uint_as_float(((unsigned)v) << 16); }
; __device__ __forceinline__ float fexp2(float x) { return __builtin_amdgcn_exp2f(x); }
; __device__ __forceinline__ float sigmoidf_(float x) { return __builtin_amdgcn_rcpf(1.f + fexp(-x)); }
; #define MFMA32(a, b, c) __builtin_amdgcn_mfma_f32_16x16x32_bf16((a), (b), (c), 0, 0, 0)
; template <int PASS>
; __device__ void lru_loop(const Params& p, int l, char* smem, int first, int end, int stride, bool skip_ctx, int oz) {
;     ...
;     for (int mt = 0; mt < 4; ++mt) {
;         f32x4 racc = {0.f, 0.f, 0.f, 0.f}, iacc = {0.f, 0.f, 0.f, 0.f};
; #pragma unroll
;         for (int s = 0; s < 2; ++s) {
;             const bf16x8 a = *(const bf16x8*)(ul + (16 * mt + li) * LS + 32 * s + 8 * g);
;             racc = MFMA32(a, wf[0][s], racc);
;             iacc = MFMA32(a, wf[1][s], iacc);
;         }
; #pragma unroll
;         for (int r = 0; r < 4; ++r) {
;             const float uval = bf2f(ul[(16 * mt + 4 * g + r) * LS + d]);
;             const float rg = sigmoidf_(racc[r] + br), ig = sigmoidf_(iacc[r] + bi);
;             const float a = fexp2(sp8 * rg);
;             av[mt][r] = a;
;             bv[mt][r] = __builtin_amdgcn_sqrtf(fmaxf(0.f, 1.f - a * a)) * ig * uval;
;         }
;     }
	v_mfma_f32_16x16x32_bf16 v[98:101], v[84:87], v[44:47], 0
	v_lshlrev_b32_e32 v80, 16, v83
	v_mul_f32_e32 v77, v77, v79
	v_mul_f32_e32 v80, v77, v80
	v_add_f32_e32 v77, 1.0, v82
	v_add_f32_e32 v79, v134, v81
	v_rcp_f32_e32 v77, v77
	v_mul_f32_e32 v79, 0xbfb8aa3b, v79
	v_exp_f32_e32 v79, v79
	s_waitcnt lgkmcnt(0)
	v_mfma_f32_16x16x32_bf16 v[98:101], v[88:91], v[48:51], v[98:101]
	v_mul_f32_e32 v77, v136, v77
	v_exp_f32_e32 v82, v77
	v_add_f32_e32 v77, 1.0, v79
	v_mfma_f32_16x16x32_bf16 v[84:87], v[84:87], v[52:55], 0
	v_rcp_f32_e32 v102, v77
	s_nop 2
	v_add_f32_e32 v79, v1, v98
	v_mul_f32_e32 v79, 0xbfb8aa3b, v79
	v_exp_f32_e32 v79, v79
	v_mfma_f32_16x16x32_bf16 v[84:87], v[88:91], v[56:59], v[84:87]
	v_fma_f32 v77, -v82, v82, 1.0
	v_max_f32_e32 v77, 0, v77
	v_add_f32_e32 v79, 1.0, v79
	v_rcp_f32_e32 v79, v79
	v_sqrt_f32_e32 v88, v77
	s_nop 2
	v_add_f32_e32 v81, v134, v84
	v_mul_f32_e32 v81, 0xbfb8aa3b, v81
	v_exp_f32_e32 v81, v81
	v_mul_f32_e32 v79, v136, v79
	v_exp_f32_e32 v83, v79
	v_add_f32_e32 v79, v1, v99
	v_mul_f32_e32 v79, 0xbfb8aa3b, v79
	v_exp_f32_e32 v79, v79
	v_add_f32_e32 v77, 1.0, v81
	v_rcp_f32_e32 v103, v77
	v_fma_f32 v77, -v83, v83, 1.0
	v_max_f32_e32 v77, 0, v77
	v_sqrt_f32_e32 v89, v77
	v_add_f32_e32 v77, 1.0, v79
	v_rcp_f32_e32 v77, v77
	v_add_f32_e32 v79, v134, v85
	v_mul_f32_e32 v79, 0xbfb8aa3b, v79
	v_exp_f32_e32 v79, v79
	v_mul_f32_e32 v77, v136, v77
	v_exp_f32_e32 v147, v77
	v_add_f32_e32 v81, v1, v100
	v_add_f32_e32 v77, 1.0, v79
	v_mul_f32_e32 v81, 0xbfb8aa3b, v81
	v_fma_f32 v79, -v147, v147, 1.0
	v_max_f32_e32 v79, 0, v79
	v_rcp_f32_e32 v77, v77
	v_sqrt_f32_e32 v79, v79
	v_exp_f32_e32 v81, v81
	v_pk_mul_f32 v[84:85], v[102:103], v[88:89]
	v_lshlrev_b32_e32 v88, 16, v106
	v_mul_f32_e32 v77, v77, v79
	v_add_f32_e32 v79, 1.0, v81
	v_add_f32_e32 v81, v134, v86
	v_rcp_f32_e32 v79, v79
	v_mul_f32_e32 v81, 0xbfb8aa3b, v81
	v_exp_f32_e32 v81, v81
	v_mul_f32_e32 v146, v77, v88
	v_mul_f32_e32 v79, v136, v79
	v_exp_f32_e32 v148, v79
	v_add_f32_e32 v77, 1.0, v81
	v_add_f32_e32 v81, v1, v101
	ds_read_b128 v[98:101], v141 offset:4608
	v_lshlrev_b32_e32 v91, 16, v105
	v_lshlrev_b32_e32 v90, 16, v104
	v_fma_f32 v79, -v148, v148, 1.0
	ds_read_b128 v[102:105], v141 offset:4672
	v_max_f32_e32 v79, 0, v79
	v_rcp_f32_e32 v77, v77
	v_sqrt_f32_e32 v79, v79
	v_mul_f32_e32 v81, 0xbfb8aa3b, v81
	v_exp_f32_e32 v81, v81
	v_lshlrev_b32_e32 v86, 16, v107
	s_waitcnt lgkmcnt(1)
	v_mfma_f32_16x16x32_bf16 v[106:109], v[98:101], v[44:47], 0
	v_mul_f32_e32 v77, v77, v79
	v_mul_f32_e32 v86, v77, v86
	v_add_f32_e32 v77, 1.0, v81
	v_add_f32_e32 v79, v134, v87
	v_rcp_f32_e32 v77, v77
	v_mul_f32_e32 v79, 0xbfb8aa3b, v79
	v_exp_f32_e32 v79, v79
	s_waitcnt lgkmcnt(0)
	v_mfma_f32_16x16x32_bf16 v[106:109], v[102:105], v[48:51], v[106:109]
	v_mul_f32_e32 v77, v136, v77
	v_exp_f32_e32 v88, v77
	v_add_f32_e32 v77, 1.0, v79
	v_mfma_f32_16x16x32_bf16 v[98:101], v[98:101], v[52:55], 0
	v_mul_f32_e64 v84, v84, v90
	v_mul_f32_e64 v85, v85, v91
	s_nop 1
	v_add_f32_e32 v79, v1, v106
	v_mul_f32_e32 v79, 0xbfb8aa3b, v79
	v_exp_f32_e32 v79, v79
	v_mfma_f32_16x16x32_bf16 v[98:101], v[102:105], v[56:59], v[98:101]
	v_rcp_f32_e32 v90, v77
	v_fma_f32 v77, -v88, v88, 1.0
	v_add_f32_e32 v79, 1.0, v79
	v_rcp_f32_e32 v79, v79
	v_max_f32_e32 v77, 0, v77
	s_nop 2
	v_add_f32_e32 v81, v134, v98
	v_mul_f32_e32 v81, 0xbfb8aa3b, v81
	v_exp_f32_e32 v81, v81
	v_mul_f32_e32 v79, v136, v79
	v_exp_f32_e32 v89, v79
	v_sqrt_f32_e32 v102, v77
	v_add_f32_e32 v77, 1.0, v81
	v_rcp_f32_e32 v91, v77
	v_fma_f32 v77, -v89, v89, 1.0
	v_max_f32_e32 v77, 0, v77
	v_sqrt_f32_e32 v103, v77
	v_add_f32_e32 v77, v1, v107
	v_mul_f32_e32 v77, 0xbfb8aa3b, v77
	v_exp_f32_e32 v77, v77
	ds_read_u16 v79, v142 offset:4608
	ds_read_u16 v81, v142 offset:4752
	ds_read_u16 v87, v142 offset:4896
	ds_read_u16 v116, v142 offset:5040
	ds_read_u16 v117, v142 offset:6912
	ds_read_u16 v118, v142 offset:7056
	ds_read_u16 v119, v142 offset:7200
	ds_read_u16 v120, v142 offset:7344
	s_waitcnt lgkmcnt(7)
; __device__ __forceinline__ float bf2f(bf16_t v) { return __uint_as_float(((unsigned)v) << 16); }
; __device__ __forceinline__ float fexp2(float x) { return __builtin_amdgcn_exp2f(x); }
; __device__ __forceinline__ float sigmoidf_(float x) { return __builtin_amdgcn_rcpf(1.f + fexp(-x)); }
; #define MFMA32(a, b, c) __builtin_amdgcn_mfma_f32_16x16x32_bf16((a), (b), (c), 0, 0, 0)
; template <int PASS>
; __device__ void lru_loop(const Params& p, int l, char* smem, int first, int end, int stride, bool skip_ctx, int oz) {
;     ...
;     for (int mt = 0; mt < 4; ++mt) {
;         f32x4 racc = {0.f, 0.f, 0.f, 0.f}, iacc = {0.f, 0.f, 0.f, 0.f};
; #pragma unroll
;         for (int s = 0; s < 2; ++s) {
;             const bf16x8 a = *(const bf16x8*)(ul + (16 * mt + li) * LS + 32 * s + 8 * g);
;             racc = MFMA32(a, wf[0][s], racc);
;             iacc = MFMA32(a, wf[1][s], iacc);
;         }
; #pragma unroll
;         for (int r = 0; r < 4; ++r) {
;             const float uval = bf2f(ul[(16 * mt + 4 * g + r) * LS + d]);
;             const float rg = sigmoidf_(racc[r] + br), ig = sigmoidf_(iacc[r] + bi);
;             const float a = fexp2(sp8 * rg);
;             av[mt][r] = a;
;             bv[mt][r] = __builtin_amdgcn_sqrtf(fmaxf(0.f, 1.f - a * a)) * ig * uval;
;         }
;     }
;     if (PASS == 0) {
;         float hc = 0.f, pc = 1.f;
;         float pv[4][4];
;         if (dir == 0) lru_scan<0>(av, bv, hv, pv, hc, pc, g, li);
;         else          lru_scan<1>(av, bv, hv, pv, hc, pc, g, li);
	v_lshlrev_b32_e32 v105, 16, v79
	v_add_f32_e32 v79, v134, v99
	v_add_f32_e32 v77, 1.0, v77
	v_rcp_f32_e32 v77, v77
	v_mul_f32_e32 v79, 0xbfb8aa3b, v79
	v_exp_f32_e32 v79, v79
	v_add_f32_e32 v98, v1, v108
	v_mul_f32_e32 v77, v136, v77
	v_exp_f32_e32 v150, v77
	v_add_f32_e32 v77, 1.0, v79
	v_mul_f32_e32 v98, 0xbfb8aa3b, v98
	v_rcp_f32_e32 v77, v77
	v_fma_f32 v79, -v150, v150, 1.0
	v_max_f32_e32 v79, 0, v79
	v_sqrt_f32_e32 v79, v79
	v_exp_f32_e32 v98, v98
	v_lshlrev_b32_e32 v104, 16, v110
	v_pk_mul_f32 v[90:91], v[90:91], v[102:103]
	v_mul_f32_e32 v77, v77, v79
	v_add_f32_e32 v79, 1.0, v98
	v_rcp_f32_e32 v79, v79
	v_add_f32_e32 v98, v134, v100
	v_pk_mul_f32 v[90:91], v[90:91], v[104:105]
	v_mul_f32_e32 v98, 0xbfb8aa3b, v98
	v_mul_f32_e32 v79, v136, v79
	v_exp_f32_e32 v151, v79
	ds_read_b128 v[102:105], v141 offset:6912
	v_exp_f32_e32 v98, v98
	s_waitcnt lgkmcnt(7)
	v_lshlrev_b32_e32 v81, 16, v81
	v_mul_f32_e32 v149, v77, v81
	v_fma_f32 v79, -v151, v151, 1.0
	v_add_f32_e32 v81, v1, v109
	ds_read_b128 v[106:109], v141 offset:6976
	v_add_f32_e32 v77, 1.0, v98
	v_max_f32_e32 v79, 0, v79
	v_rcp_f32_e32 v77, v77
	v_sqrt_f32_e32 v79, v79
	v_mul_f32_e32 v81, 0xbfb8aa3b, v81
	v_exp_f32_e32 v81, v81
	s_waitcnt lgkmcnt(1)
	v_mfma_f32_16x16x32_bf16 v[110:113], v[102:105], v[44:47], 0
	v_lshlrev_b32_e32 v87, 16, v87
	v_mul_f32_e32 v77, v77, v79
	v_mul_f32_e32 v98, v77, v87
	v_add_f32_e32 v77, 1.0, v81
	v_add_f32_e32 v79, v134, v101
	v_rcp_f32_e32 v77, v77
	v_mul_f32_e32 v79, 0xbfb8aa3b, v79
	v_exp_f32_e32 v79, v79
	s_waitcnt lgkmcnt(0)
	v_mfma_f32_16x16x32_bf16 v[110:113], v[106:109], v[48:51], v[110:113]
	v_mul_f32_e32 v77, v136, v77
	v_exp_f32_e32 v100, v77
	v_add_f32_e32 v77, 1.0, v79
	v_mfma_f32_16x16x32_bf16 v[102:105], v[102:105], v[52:55], 0
	v_rcp_f32_e32 v114, v77
	s_nop 2
	v_add_f32_e32 v79, v1, v110
	v_mul_f32_e32 v79, 0xbfb8aa3b, v79
	v_exp_f32_e32 v79, v79
	v_mfma_f32_16x16x32_bf16 v[102:105], v[106:109], v[56:59], v[102:105]
	v_fma_f32 v77, -v100, v100, 1.0
	v_max_f32_e32 v77, 0, v77
	v_add_f32_e32 v79, 1.0, v79
	v_rcp_f32_e32 v79, v79
	v_sqrt_f32_e32 v106, v77
	s_nop 2
	v_add_f32_e32 v81, v134, v102
	v_mul_f32_e32 v81, 0xbfb8aa3b, v81
	v_exp_f32_e32 v81, v81
	v_mul_f32_e32 v79, v136, v79
	v_exp_f32_e32 v101, v79
	v_add_f32_e32 v79, v1, v111
	v_mul_f32_e32 v79, 0xbfb8aa3b, v79
	v_exp_f32_e32 v79, v79
	v_add_f32_e32 v77, 1.0, v81
	v_rcp_f32_e32 v115, v77
	v_fma_f32 v77, -v101, v101, 1.0
	v_max_f32_e32 v77, 0, v77
	v_sqrt_f32_e32 v107, v77
	v_add_f32_e32 v77, 1.0, v79
	v_rcp_f32_e32 v77, v77
	v_add_f32_e32 v79, v134, v103
	v_mul_f32_e32 v79, 0xbfb8aa3b, v79
	v_exp_f32_e32 v79, v79
	v_mul_f32_e32 v77, v136, v77
	v_exp_f32_e32 v152, v77
	v_add_f32_e32 v81, v1, v112
	v_add_f32_e32 v77, 1.0, v79
	v_mul_f32_e32 v81, 0xbfb8aa3b, v81
	v_fma_f32 v79, -v152, v152, 1.0
	v_max_f32_e32 v79, 0, v79
	v_rcp_f32_e32 v77, v77
	v_sqrt_f32_e32 v79, v79
	v_exp_f32_e32 v81, v81
	v_lshlrev_b32_e32 v87, 16, v118
	v_lshlrev_b32_e32 v109, 16, v117
	v_mul_f32_e32 v77, v77, v79
	v_add_f32_e32 v79, 1.0, v81
	v_rcp_f32_e32 v79, v79
	v_mul_f32_e32 v153, v77, v87
	v_add_f32_e32 v81, v134, v104
	v_mul_f32_e32 v81, 0xbfb8aa3b, v81
	v_mul_f32_e32 v77, v136, v79
	v_add_f32_e32 v79, v1, v113
	v_mul_f32_e32 v79, 0xbfb8aa3b, v79
	v_exp_f32_e32 v79, v79
	v_exp_f32_e32 v77, v77
	v_add_f32_e32 v104, v134, v105
	v_exp_f32_e32 v81, v81
	v_add_f32_e32 v79, 1.0, v79
	v_rcp_f32_e32 v79, v79
	v_mul_f32_e32 v104, 0xbfb8aa3b, v104
	v_exp_f32_e32 v104, v104
	v_fma_f32 v99, -v77, v77, 1.0
	v_mul_f32_e32 v79, v136, v79
	v_exp_f32_e32 v79, v79
	v_add_f32_e32 v81, 1.0, v81
	v_max_f32_e32 v99, 0, v99
	v_rcp_f32_e32 v81, v81
	v_fma_f32 v105, -v79, v79, 1.0
	v_sqrt_f32_e32 v99, v99
	v_add_f32_e32 v104, 1.0, v104
	v_max_f32_e32 v105, 0, v105
	v_rcp_f32_e32 v104, v104
	v_sqrt_f32_e32 v105, v105
	v_lshlrev_b32_e32 v87, 16, v119
	v_mul_f32_e32 v81, v81, v99
	v_lshlrev_b32_e32 v108, 16, v116
	v_pk_mul_f32 v[102:103], v[114:115], v[106:107]
	v_mul_f32_e32 v154, v81, v87
	v_lshlrev_b32_e32 v81, 16, v120
	v_mul_f32_e32 v87, v104, v105
	v_pk_mul_f32 v[102:103], v[102:103], v[108:109]
	v_mul_f32_e32 v155, v87, v81
	s_cbranch_vccnz .LBB0_731
	s_andn2_b64 vcc, exec, s[0:1]
	s_cbranch_vccz .LBB0_732
